# best version plus exec-masking of the y-writer's now-unused centroid gathers in scan 1 (removes 24 MB of L2 reads)
# speedup vs baseline: 1.0135x; 1.0035x over previous
.LBB1_100:
	s_and_b32 s4, s99, 0xffff8000
	s_mov_b64 s[96:97], s[14:15]
	s_mov_b64 s[92:93], s[18:19]
	s_add_i32 s4, vcc_lo, s4
	s_mov_b32 s95, s5
	s_mov_b32 s89, s5
	s_mov_b32 s87, s5
	s_mov_b32 s83, s5
	s_mov_b32 s79, s5
	s_mov_b32 s77, s5
	s_mov_b32 s73, s5
	s_mov_b32 s69, s5
	s_mov_b32 s65, s5
	s_mov_b32 s63, s5
	s_mov_b32 s61, s5
	s_mov_b32 s59, s5
	s_mov_b32 s57, s5
	s_mov_b32 s55, s5
	s_mov_b32 s49, s5
	s_add_i32 s94, s4, 1
	s_add_i32 s88, s4, 2
	s_add_i32 s86, s4, 3
	s_add_i32 s82, s4, 4
	s_add_i32 s78, s4, 5
	s_add_i32 s76, s4, 6
	s_add_i32 s72, s4, 7
	s_add_i32 s68, s4, 8
	s_add_i32 s64, s4, 9
	s_add_i32 s62, s4, 10
	s_add_i32 s60, s4, 11
	s_add_i32 s58, s4, 12
	s_add_i32 s56, s4, 13
	s_add_i32 s54, s4, 14
	s_add_i32 s48, s4, 15
	v_mov_b32_e32 v1, s3
	v_lshl_add_u64 v[132:133], s[96:97], 0, v[162:163]
	v_lshl_add_u64 v[130:131], s[92:93], 0, v[162:163]
	s_lshl_b64 s[92:93], s[4:5], 10
	s_lshl_b64 s[94:95], s[94:95], 10
	s_lshl_b64 s[88:89], s[88:89], 10
	s_lshl_b64 s[86:87], s[86:87], 10
	s_lshl_b64 s[82:83], s[82:83], 10
	s_lshl_b64 s[78:79], s[78:79], 10
	s_lshl_b64 s[76:77], s[76:77], 10
	s_lshl_b64 s[72:73], s[72:73], 10
	s_lshl_b64 s[68:69], s[68:69], 10
	s_lshl_b64 s[64:65], s[64:65], 10
	s_lshl_b64 s[62:63], s[62:63], 10
	s_lshl_b64 s[60:61], s[60:61], 10
	s_lshl_b64 s[58:59], s[58:59], 10
	s_lshl_b64 s[56:57], s[56:57], 10
	s_lshl_b64 s[54:55], s[54:55], 10
	s_lshl_b64 s[48:49], s[48:49], 10
	v_lshl_add_u64 v[144:145], v[132:133], 0, s[92:93]
	v_lshl_add_u64 v[146:147], v[132:133], 0, s[94:95]
	v_lshl_add_u64 v[148:149], v[132:133], 0, s[88:89]
	v_lshl_add_u64 v[150:151], v[132:133], 0, s[86:87]
	v_lshl_add_u64 v[152:153], v[132:133], 0, s[82:83]
	v_lshl_add_u64 v[154:155], v[132:133], 0, s[78:79]
	v_lshl_add_u64 v[156:157], v[132:133], 0, s[76:77]
	v_lshl_add_u64 v[158:159], v[132:133], 0, s[72:73]
	v_lshl_add_u64 v[160:161], v[132:133], 0, s[68:69]
	v_lshl_add_u64 v[166:167], v[132:133], 0, s[64:65]
	v_lshl_add_u64 v[168:169], v[132:133], 0, s[62:63]
	v_lshl_add_u64 v[170:171], v[132:133], 0, s[60:61]
	v_lshl_add_u64 v[172:173], v[132:133], 0, s[58:59]
	v_lshl_add_u64 v[174:175], v[132:133], 0, s[56:57]
	v_lshl_add_u64 v[176:177], v[132:133], 0, s[54:55]
	v_lshl_add_u64 v[178:179], v[132:133], 0, s[48:49]
	ds_read_b128 v[132:135], v1
	ds_read_b128 v[136:139], v1 offset:16
	s_mov_b32 s53, s5
	s_mov_b32 s7, s5
	s_mov_b32 s9, s5
	s_waitcnt lgkmcnt(1)
	v_readfirstlane_b32 s52, v132
	v_readfirstlane_b32 s50, v133
	v_readfirstlane_b32 s46, v134
	v_readfirstlane_b32 s44, v135
	ds_read_b128 v[132:135], v1 offset:32
	ds_read_b128 v[140:143], v1 offset:48
	s_mov_b32 s11, s5
	s_mov_b32 s13, s5
	s_mov_b32 s27, s5
	s_mov_b32 s29, s5
	s_mov_b32 s35, s5
	s_mov_b32 s37, s5
	s_mov_b32 s39, s5
	s_waitcnt lgkmcnt(2)
	v_readfirstlane_b32 s6, v137
	v_readfirstlane_b32 s8, v138
	v_readfirstlane_b32 s10, v139
	s_waitcnt lgkmcnt(1)
	v_readfirstlane_b32 s12, v132
	v_readfirstlane_b32 s26, v133
	v_readfirstlane_b32 s28, v134
	v_readfirstlane_b32 s34, v135
	s_waitcnt lgkmcnt(0)
	v_readfirstlane_b32 s36, v140
	v_readfirstlane_b32 s38, v141
	s_mov_b32 s51, s5
	s_mov_b32 s47, s5
	s_mov_b32 s45, s5
	s_mov_b32 s31, s5
	s_mov_b32 s41, s5
	s_mov_b32 s43, s5
	s_lshl_b64 s[52:53], s[52:53], 10
	v_readfirstlane_b32 s30, v136
	v_readfirstlane_b32 s40, v142
	v_readfirstlane_b32 s42, v143
	s_lshl_b64 s[6:7], s[6:7], 10
	s_lshl_b64 s[8:9], s[8:9], 10
	s_lshl_b64 s[10:11], s[10:11], 10
	s_lshl_b64 s[12:13], s[12:13], 10
	s_lshl_b64 s[26:27], s[26:27], 10
	s_lshl_b64 s[28:29], s[28:29], 10
	s_lshl_b64 s[34:35], s[34:35], 10
	s_lshl_b64 s[36:37], s[36:37], 10
	s_lshl_b64 s[38:39], s[38:39], 10
	v_lshl_add_u64 v[180:181], v[130:131], 0, s[52:53]
	s_lshl_b64 s[50:51], s[50:51], 10
	s_lshl_b64 s[46:47], s[46:47], 10
	s_lshl_b64 s[44:45], s[44:45], 10
	s_lshl_b64 s[30:31], s[30:31], 10
	s_mov_b64 exec, 0
	s_waitcnt vmcnt(31)
	global_store_dwordx4 v[144:145], v[26:29], off nt
	s_waitcnt vmcnt(31)
	global_store_dwordx4 v[146:147], v[18:21], off nt
	s_waitcnt vmcnt(31)
	global_store_dwordx4 v[148:149], v[10:13], off nt
	s_waitcnt vmcnt(23)
	global_store_dwordx4 v[150:151], v[2:5], off nt
	global_store_dwordx4 v[152:153], v[30:33], off nt
	global_store_dwordx4 v[154:155], v[14:17], off nt
	s_waitcnt vmcnt(25)
	global_store_dwordx4 v[156:157], v[6:9], off nt
	s_waitcnt vmcnt(25)
	global_store_dwordx4 v[158:159], v[22:25], off nt
	global_store_dwordx4 v[160:161], v[58:61], off nt
	global_store_dwordx4 v[166:167], v[54:57], off nt
	global_store_dwordx4 v[168:169], v[46:49], off nt
	s_waitcnt vmcnt(28)
	global_store_dwordx4 v[170:171], v[34:37], off nt
	global_store_dwordx4 v[172:173], v[62:65], off nt
	global_store_dwordx4 v[174:175], v[50:53], off nt
	global_store_dwordx4 v[176:177], v[42:45], off nt
	s_waitcnt vmcnt(31)
	global_store_dwordx4 v[178:179], v[38:41], off nt
	s_mov_b64 exec, -1
	s_lshl_b64 s[40:41], s[40:41], 10
	s_lshl_b64 s[42:43], s[42:43], 10
	v_lshl_add_u64 v[6:7], v[130:131], 0, s[6:7]
	v_lshl_add_u64 v[8:9], v[130:131], 0, s[8:9]
	v_lshl_add_u64 v[22:23], v[130:131], 0, s[10:11]
	v_lshl_add_u64 v[34:35], v[130:131], 0, s[12:13]
	v_lshl_add_u64 v[36:37], v[130:131], 0, s[26:27]
	v_lshl_add_u64 v[38:39], v[130:131], 0, s[28:29]
	v_lshl_add_u64 v[40:41], v[130:131], 0, s[34:35]
	v_lshl_add_u64 v[42:43], v[130:131], 0, s[36:37]
	v_lshl_add_u64 v[44:45], v[130:131], 0, s[38:39]
	v_lshl_add_u64 v[182:183], v[130:131], 0, s[50:51]
	v_lshl_add_u64 v[184:185], v[130:131], 0, s[46:47]
	v_lshl_add_u64 v[186:187], v[130:131], 0, s[44:45]
	v_lshl_add_u64 v[188:189], v[130:131], 0, s[30:31]
	v_lshl_add_u64 v[132:133], v[130:131], 0, s[40:41]
	v_lshl_add_u64 v[130:131], v[130:131], 0, s[42:43]
	s_cmp_lt_u32 vcc_hi, 4
	s_cselect_b64 exec, 0, -1
	global_load_dwordx4 v[26:29], v[180:181], off
	global_load_dwordx4 v[18:21], v[182:183], off
	global_load_dwordx4 v[10:13], v[184:185], off
	global_load_dwordx4 v[2:5], v[186:187], off
	global_load_dwordx4 v[30:33], v[188:189], off
	global_load_dwordx4 v[14:17], v[6:7], off
	s_nop 0
	global_load_dwordx4 v[6:9], v[8:9], off
	s_nop 0
	global_load_dwordx4 v[22:25], v[22:23], off
	s_nop 0
	global_load_dwordx4 v[58:61], v[34:35], off
	global_load_dwordx4 v[54:57], v[36:37], off
	global_load_dwordx4 v[46:49], v[38:39], off
	s_nop 0
	global_load_dwordx4 v[34:37], v[40:41], off
	global_load_dwordx4 v[62:65], v[42:43], off
	global_load_dwordx4 v[50:53], v[44:45], off
	s_nop 0
	global_load_dwordx4 v[42:45], v[132:133], off
	global_load_dwordx4 v[38:41], v[130:131], off
	s_mov_b64 exec, -1
	s_mov_b64 s[22:23], s[14:15]
	s_mov_b64 s[24:25], s[18:19]
	s_barrier
	ds_read_b128 v[130:133], v1 offset:64
	ds_read_b128 v[134:137], v1 offset:80
	ds_read_b128 v[138:141], v1 offset:96
	ds_read_b128 v[142:145], v1 offset:112
	s_mov_b32 s67, s5
	s_add_i32 s66, s4, 16
	s_add_i32 s70, s4, 17
	s_add_i32 s74, s4, 18
	s_add_i32 s80, s4, 19
	s_add_i32 s84, s4, 20
	s_add_i32 s90, s4, 21
	s_add_i32 s96, s4, 22
	s_add_i32 s92, s4, 23
	s_add_i32 s94, s4, 24
	s_add_i32 s88, s4, 25
	s_add_i32 s86, s4, 26
	s_add_i32 s82, s4, 27
	s_add_i32 s78, s4, 28
	s_add_i32 s76, s4, 29
	s_add_i32 s72, s4, 30
	s_add_i32 s4, s4, 31
	s_mov_b32 s71, s5
	s_mov_b32 s75, s5
	s_mov_b32 s81, s5
	s_mov_b32 s85, s5
	s_mov_b32 s91, s5
	s_mov_b32 s97, s5
	s_mov_b32 s93, s5
	s_mov_b32 s95, s5
	s_mov_b32 s89, s5
	s_mov_b32 s87, s5
	s_mov_b32 s83, s5
	s_mov_b32 s79, s5
	s_mov_b32 s77, s5
	s_mov_b32 s73, s5
	s_lshl_b64 s[66:67], s[66:67], 10
	s_lshl_b64 s[30:31], s[4:5], 10
	v_lshl_add_u64 v[146:147], s[22:23], 0, v[162:163]
	s_waitcnt lgkmcnt(3)
	v_readfirstlane_b32 s4, v130
	s_mov_b32 s69, s5
	s_mov_b32 s65, s5
	s_mov_b32 s63, s5
	s_mov_b32 s61, s5
	s_mov_b32 s59, s5
	s_mov_b32 s57, s5
	s_mov_b32 s55, s5
	s_mov_b32 s49, s5
	s_mov_b32 s53, s5
	s_mov_b32 s51, s5
	s_mov_b32 s47, s5
	s_mov_b32 s45, s5
	s_lshl_b64 s[70:71], s[70:71], 10
	s_lshl_b64 s[74:75], s[74:75], 10
	s_lshl_b64 s[80:81], s[80:81], 10
	s_lshl_b64 s[84:85], s[84:85], 10
	s_lshl_b64 s[90:91], s[90:91], 10
	s_lshl_b64 s[96:97], s[96:97], 10
	s_lshl_b64 s[92:93], s[92:93], 10
	s_lshl_b64 s[94:95], s[94:95], 10
	s_lshl_b64 s[88:89], s[88:89], 10
	s_lshl_b64 s[86:87], s[86:87], 10
	s_lshl_b64 s[82:83], s[82:83], 10
	s_lshl_b64 s[78:79], s[78:79], 10
	s_lshl_b64 s[76:77], s[76:77], 10
	s_lshl_b64 s[72:73], s[72:73], 10
	v_lshl_add_u64 v[148:149], s[24:25], 0, v[162:163]
	v_lshl_add_u64 v[150:151], v[146:147], 0, s[66:67]
	v_readfirstlane_b32 s68, v131
	v_readfirstlane_b32 s64, v132
	v_readfirstlane_b32 s62, v133
	s_waitcnt lgkmcnt(2)
	v_readfirstlane_b32 s60, v135
	v_readfirstlane_b32 s58, v136
	v_readfirstlane_b32 s56, v137
	s_waitcnt lgkmcnt(1)
	v_readfirstlane_b32 s54, v139
	v_readfirstlane_b32 s48, v140
	v_readfirstlane_b32 s52, v141
	s_waitcnt lgkmcnt(0)
	v_readfirstlane_b32 s50, v143
	v_readfirstlane_b32 s46, v144
	v_readfirstlane_b32 s44, v145
	s_lshl_b64 s[6:7], s[4:5], 10
	v_readfirstlane_b32 s4, v134
	v_lshl_add_u64 v[152:153], v[146:147], 0, s[70:71]
	v_lshl_add_u64 v[154:155], v[146:147], 0, s[74:75]
	v_lshl_add_u64 v[156:157], v[146:147], 0, s[80:81]
	v_lshl_add_u64 v[158:159], v[146:147], 0, s[84:85]
	v_lshl_add_u64 v[160:161], v[146:147], 0, s[90:91]
	v_lshl_add_u64 v[166:167], v[146:147], 0, s[96:97]
	v_lshl_add_u64 v[168:169], v[146:147], 0, s[92:93]
	v_lshl_add_u64 v[170:171], v[146:147], 0, s[94:95]
	v_lshl_add_u64 v[172:173], v[146:147], 0, s[88:89]
	v_lshl_add_u64 v[174:175], v[146:147], 0, s[86:87]
	v_lshl_add_u64 v[176:177], v[146:147], 0, s[82:83]
	v_lshl_add_u64 v[178:179], v[146:147], 0, s[78:79]
	v_lshl_add_u64 v[180:181], v[146:147], 0, s[76:77]
	v_lshl_add_u64 v[182:183], v[146:147], 0, s[72:73]
	v_lshl_add_u64 v[146:147], v[146:147], 0, s[30:31]
	s_mov_b64 exec, 0
	s_waitcnt vmcnt(47)
	global_store_dwordx4 v[150:151], v[78:81], off nt
	s_waitcnt vmcnt(47)
	global_store_dwordx4 v[152:153], v[74:77], off nt
	s_waitcnt vmcnt(47)
	global_store_dwordx4 v[154:155], v[70:73], off nt
	s_waitcnt vmcnt(40)
	global_store_dwordx4 v[156:157], v[66:69], off nt
	s_waitcnt vmcnt(38)
	global_store_dwordx4 v[158:159], v[118:121], off nt
	global_store_dwordx4 v[160:161], v[86:89], off nt
	s_waitcnt vmcnt(42)
	global_store_dwordx4 v[166:167], v[82:85], off nt
	s_waitcnt vmcnt(42)
	global_store_dwordx4 v[168:169], v[90:93], off nt
	s_waitcnt vmcnt(41)
	global_store_dwordx4 v[170:171], v[126:129], off nt
	global_store_dwordx4 v[172:173], v[102:105], off nt
	global_store_dwordx4 v[174:175], v[98:101], off nt
	s_waitcnt vmcnt(45)
	global_store_dwordx4 v[176:177], v[94:97], off nt
	s_waitcnt vmcnt(44)
	global_store_dwordx4 v[178:179], v[122:125], off nt
	global_store_dwordx4 v[180:181], v[110:113], off nt
	s_waitcnt vmcnt(47)
	global_store_dwordx4 v[182:183], v[106:109], off nt
	s_waitcnt vmcnt(47)
	global_store_dwordx4 v[146:147], v[114:117], off nt
	s_mov_b64 exec, -1
	s_lshl_b64 s[8:9], s[68:69], 10
	s_lshl_b64 s[10:11], s[64:65], 10
	s_lshl_b64 s[12:13], s[62:63], 10
	s_lshl_b64 s[22:23], s[60:61], 10
	s_lshl_b64 s[24:25], s[58:59], 10
	s_lshl_b64 s[26:27], s[56:57], 10
	s_lshl_b64 s[28:29], s[54:55], 10
	s_lshl_b64 s[30:31], s[48:49], 10
	s_lshl_b64 s[34:35], s[52:53], 10
	s_lshl_b64 s[36:37], s[50:51], 10
	s_lshl_b64 s[38:39], s[46:47], 10
	s_lshl_b64 s[40:41], s[44:45], 10
	v_lshl_add_u64 v[66:67], v[148:149], 0, s[6:7]
	s_lshl_b64 s[6:7], s[4:5], 10
	v_lshl_add_u64 v[82:83], v[148:149], 0, s[8:9]
	v_lshl_add_u64 v[84:85], v[148:149], 0, s[10:11]
	v_lshl_add_u64 v[86:87], v[148:149], 0, s[12:13]
	v_lshl_add_u64 v[94:95], v[148:149], 0, s[22:23]
	v_lshl_add_u64 v[96:97], v[148:149], 0, s[24:25]
	v_lshl_add_u64 v[98:99], v[148:149], 0, s[26:27]
	v_lshl_add_u64 v[106:107], v[148:149], 0, s[28:29]
	v_lshl_add_u64 v[108:109], v[148:149], 0, s[30:31]
	v_lshl_add_u64 v[110:111], v[148:149], 0, s[34:35]
	v_lshl_add_u64 v[114:115], v[148:149], 0, s[36:37]
	v_lshl_add_u64 v[116:117], v[148:149], 0, s[38:39]
	v_lshl_add_u64 v[118:119], v[148:149], 0, s[40:41]
	v_lshl_add_u64 v[120:121], v[148:149], 0, s[6:7]
	v_readfirstlane_b32 s4, v138
	s_cmp_lt_u32 vcc_hi, 4
	s_cselect_b64 exec, 0, -1
	global_load_dwordx4 v[78:81], v[66:67], off
	global_load_dwordx4 v[74:77], v[82:83], off
	global_load_dwordx4 v[70:73], v[84:85], off
	s_nop 0
	global_load_dwordx4 v[66:69], v[86:87], off
	s_nop 0
	global_load_dwordx4 v[86:89], v[94:95], off
	global_load_dwordx4 v[82:85], v[96:97], off
	global_load_dwordx4 v[90:93], v[98:99], off
	global_load_dwordx4 v[102:105], v[106:107], off
	s_nop 0
	global_load_dwordx4 v[98:101], v[108:109], off
	global_load_dwordx4 v[94:97], v[110:111], off
	s_nop 0
	global_load_dwordx4 v[110:113], v[114:115], off
	global_load_dwordx4 v[106:109], v[116:117], off
	s_nop 0
	global_load_dwordx4 v[114:117], v[118:119], off
	s_nop 0
	global_load_dwordx4 v[118:121], v[120:121], off
	s_lshl_b64 s[6:7], s[4:5], 10
	v_readfirstlane_b32 s4, v142
	v_lshl_add_u64 v[122:123], v[148:149], 0, s[6:7]
	s_lshl_b64 s[6:7], s[4:5], 10
	global_load_dwordx4 v[126:129], v[122:123], off
	v_lshl_add_u64 v[122:123], v[148:149], 0, s[6:7]
	global_load_dwordx4 v[122:125], v[122:123], off
	s_mov_b64 exec, -1
	s_add_i32 vcc_hi, vcc_hi, 2
	s_addk_i32 s99, 0x2000
	s_addk_i32 s3, 0x80
	s_add_i32 vcc_lo, vcc_lo, 32
	s_cmp_gt_u32 vcc_hi, 5
	s_waitcnt vmcnt(63) expcnt(7) lgkmcnt(15)
	s_barrier
	s_cbranch_scc0 .LBB1_100
	v_mov_b32_e32 v1, 0x22634
	s_barrier
	ds_read_b32 v130, v1
	s_waitcnt lgkmcnt(0)
	v_cmp_gt_i32_e32 vcc, 1, v130
	s_cbranch_vccnz .LBB1_104
